# speedup vs baseline: 1.0054x; 1.0054x over previous
.LBB0_34:
	s_lshr_b32 s0, s2, 2
	s_and_b32 s0, s0, 0x3ffffffe
	s_and_b32 s1, s2, 1
	v_lshrrev_b32_e32 v143, 7, v0
	s_bfe_u32 s3, s2, 0x20001
	s_or_b32 s0, s0, s1
	v_lshl_or_b32 v133, s0, 1, v143
	s_mul_i32 s0, s3, 0xc0
	v_bfe_u32 v135, v0, 6, 1
	s_movk_i32 s1, 0x60
	v_mov_b32_e32 v2, s0
	v_lshrrev_b32_e32 v3, 2, v0
	v_mad_u32_u24 v2, v135, s1, v2
	v_and_b32_e32 v142, 8, v3
	v_or_b32_e32 v2, v2, v142
	v_lshl_add_u32 v130, v2, 7, v133
	v_mov_b32_e32 v131, 0
	v_lshlrev_b64 v[2:3], 9, v[130:131]
	v_mul_u32_u24_e32 v4, 0x60, v135
	s_waitcnt lgkmcnt(0)
	v_lshl_add_u64 v[2:3], s[4:5], 0, v[2:3]
	v_lshlrev_b32_e32 v130, 4, v1
	v_lshl_add_u64 v[136:137], v[2:3], 0, v[130:131]
	v_lshlrev_b32_e32 v130, 2, v4
	v_lshl_add_u64 v[2:3], s[6:7], 0, v[130:131]
	s_movk_i32 s2, 0x300
	v_mad_u64_u32 v[4:5], s[0:1], v11, s2, v[2:3]
	v_mad_u64_u32 v[2:3], s[0:1], v10, s2, v[2:3]
	s_mov_b32 s0, 0x10000
	s_nop 0
	v_add_co_u32_e32 v14, vcc, s0, v136
	s_mov_b32 s0, 0x20000
	s_nop 0
	v_addc_co_u32_e32 v15, vcc, 0, v137, vcc
	v_add_co_u32_e32 v32, vcc, s0, v136
	v_lshlrev_b32_e32 v130, 2, v142
	s_nop 0
	v_addc_co_u32_e32 v33, vcc, 0, v137, vcc
	s_mov_b32 s0, 0x30000
	v_lshl_add_u64 v[140:141], v[2:3], 0, v[130:131]
	v_add_co_u32_e32 v2, vcc, s0, v136
	s_mov_b32 s0, 0x40000
	s_nop 0
	v_addc_co_u32_e32 v3, vcc, 0, v137, vcc
	v_lshl_add_u64 v[138:139], v[4:5], 0, v[130:131]
	v_add_co_u32_e32 v4, vcc, s0, v136
	s_mov_b32 s0, 0x50000
	s_nop 0
	v_addc_co_u32_e32 v5, vcc, 0, v137, vcc
	v_add_co_u32_e32 v34, vcc, s0, v136
	global_load_dwordx4 v[16:19], v[2:3], off
	global_load_dwordx4 v[20:23], v[4:5], off
	s_nop 0
	global_load_dwordx4 v[2:5], v[140:141], off offset:16
	global_load_dwordx4 v[6:9], v[140:141], off
	global_load_dwordx4 v[10:13], v[138:139], off offset:16
	global_load_dwordx4 v[24:27], v[138:139], off
	v_addc_co_u32_e32 v35, vcc, 0, v137, vcc
	s_mov_b32 s0, 0x60000
	v_add_co_u32_e32 v36, vcc, s0, v136
	s_mov_b32 s0, 0x70000
	s_nop 0
	v_addc_co_u32_e32 v37, vcc, 0, v137, vcc
	global_load_dwordx4 v[28:31], v[34:35], off
	global_load_dwordx4 v[48:51], v[36:37], off
	v_add_co_u32_e32 v34, vcc, s0, v136
	s_mov_b32 s0, 0x100000
	s_nop 0
	v_addc_co_u32_e32 v35, vcc, 0, v137, vcc
	global_load_dwordx4 v[52:55], v[34:35], off
	global_load_dwordx4 v[56:59], v[14:15], off
	global_load_dwordx4 v[60:63], v[32:33], off
	global_load_dwordx4 v[144:147], v[136:137], off
	s_mov_b32 s2, 0xffff
	s_lshl_b32 s3, s3, 16
	s_or_b32 s4, s3, 0x4000
	s_or_b32 s5, s3, 0x8000
	s_or_b32 s6, s3, 0xc000
	s_waitcnt vmcnt(9)
	v_pk_mul_f32 v[2:3], v[2:3], v[132:133] op_sel_hi:[1,0]
	s_waitcnt vmcnt(8)
	v_pk_mul_f32 v[6:7], v[6:7], v[132:133] op_sel_hi:[1,0]
	v_pk_mul_f32 v[8:9], v[8:9], v[132:133] op_sel_hi:[1,0]
	v_pk_mul_f32 v[4:5], v[4:5], v[132:133] op_sel_hi:[1,0]
	s_waitcnt vmcnt(6)
	v_pk_mul_f32 v[14:15], v[24:25], v[134:135] op_sel_hi:[1,0]
	v_pk_mul_f32 v[32:33], v[26:27], v[134:135] op_sel_hi:[1,0]
	v_pk_mul_f32 v[10:11], v[10:11], v[134:135] op_sel_hi:[1,0]
	v_cvt_pk_f16_f32 v24, v6, v7
	v_pk_mul_f32 v[6:7], v[12:13], v[134:135] op_sel_hi:[1,0]
	v_cvt_pk_f16_f32 v25, v8, v9
	v_cvt_pk_f16_f32 v26, v2, v3
	v_cvt_pk_f16_f32 v27, v4, v5
	v_cvt_pk_f16_f32 v148, v14, v15
	v_cvt_pk_f16_f32 v149, v32, v33
	v_cvt_pk_f16_f32 v150, v10, v11
	v_cvt_pk_f16_f32 v151, v6, v7
	v_add_co_u32_e32 v2, vcc, s0, v136
	s_mov_b32 s0, 0x110000
	s_nop 0
	v_addc_co_u32_e32 v3, vcc, 0, v137, vcc
	global_load_dwordx4 v[152:155], v[2:3], off
	s_waitcnt vmcnt(4)
	v_cvt_pk_f16_f32 v5, v48, v52
	v_cvt_pk_f16_f32 v4, v20, v28
	s_waitcnt vmcnt(2)
	v_cvt_pk_f16_f32 v3, v60, v16
	s_waitcnt vmcnt(1)
	v_cvt_pk_f16_f32 v2, v144, v56
	v_cvt_pk_f16_f32 v84, v22, v30
	v_add_co_u32_e32 v22, vcc, s0, v136
	v_mfma_f32_32x32x16_f16 v[98:113], v[24:27], v[2:5], 0
	v_cvt_pk_f16_f32 v85, v50, v54
	v_cvt_pk_f16_f32 v83, v62, v18
	v_cvt_pk_f16_f32 v82, v146, v58
	v_cvt_pk_f16_f32 v20, v23, v31
	v_cvt_pk_f16_f32 v19, v63, v19
	v_cvt_pk_f16_f32 v18, v147, v59
	v_addc_co_u32_e32 v23, vcc, 0, v137, vcc
	v_mfma_f32_32x32x16_f16 v[66:81], v[148:151], v[2:5], 0
	v_cvt_pk_f16_f32 v5, v49, v53
	v_cvt_pk_f16_f32 v4, v21, v29
	v_cvt_pk_f16_f32 v3, v61, v17
	v_cvt_pk_f16_f32 v2, v145, v57
	v_cvt_pk_f16_f32 v21, v51, v55
	s_mov_b32 s0, 0x120000
	global_load_dwordx4 v[144:147], v[140:141], off offset:80
	global_load_dwordx4 v[156:159], v[140:141], off offset:64
	v_mfma_f32_32x32x16_f16 v[34:49], v[24:27], v[2:5], 0
	global_load_dwordx4 v[160:163], v[138:139], off offset:80
	global_load_dwordx4 v[164:167], v[138:139], off offset:64
	s_waitcnt vmcnt(3)
	v_mul_f32_e64 v144, v144, v132
	v_mul_f32_e64 v145, v145, v132
	v_mfma_f32_32x32x16_f16 v[114:129], v[24:27], v[82:85], 0
	v_mfma_f32_32x32x16_f16 v[50:65], v[24:27], v[18:21], 0
	v_add_co_u32_e32 v24, vcc, s0, v136
	s_mov_b32 s0, 0x130000
	s_nop 0
	v_addc_co_u32_e32 v25, vcc, 0, v137, vcc
	v_add_co_u32_e32 v26, vcc, s0, v136
	s_mov_b32 s0, 0x140000
	s_nop 0
	v_addc_co_u32_e32 v27, vcc, 0, v137, vcc
	v_add_co_u32_e32 v28, vcc, s0, v136
	s_mov_b32 s0, 0x150000
	s_nop 0
	v_addc_co_u32_e32 v29, vcc, 0, v137, vcc
	v_add_co_u32_e32 v30, vcc, s0, v136
	s_mov_b32 s0, 0x160000
	s_nop 0
	v_addc_co_u32_e32 v31, vcc, 0, v137, vcc
	v_add_co_u32_e32 v32, vcc, s0, v136
	s_mov_b32 s0, 0x170000
	s_nop 0
	v_addc_co_u32_e32 v33, vcc, 0, v137, vcc
	global_load_dwordx4 v[168:171], v[30:31], off
	global_load_dwordx4 v[172:175], v[32:33], off
	v_add_co_u32_e32 v30, vcc, s0, v136
	v_mfma_f32_32x32x16_f16 v[2:17], v[148:151], v[2:5], 0
	s_nop 0
	v_addc_co_u32_e32 v31, vcc, 0, v137, vcc
	global_load_dwordx4 v[176:179], v[30:31], off
	global_load_dwordx4 v[180:183], v[26:27], off
	global_load_dwordx4 v[184:187], v[28:29], off
	global_load_dwordx4 v[188:191], v[24:25], off
	global_load_dwordx4 v[192:195], v[22:23], off
	s_mov_b32 s0, 0x200000
	v_mfma_f32_32x32x16_f16 v[82:97], v[148:151], v[82:85], 0
	v_mfma_f32_32x32x16_f16 v[18:33], v[148:151], v[18:21], 0
	s_waitcnt vmcnt(9)
	v_mul_f32_e64 v148, v156, v132
	v_mul_f32_e64 v149, v157, v132
	v_mul_f32_e64 v150, v158, v132
	v_mul_f32_e64 v151, v159, v132
	v_cvt_pk_f16_f32 v148, v148, v149
	v_cvt_pk_f16_f32 v149, v150, v151
	v_cvt_pk_f16_f32 v150, v144, v145
	v_pk_mul_f32 v[144:145], v[146:147], v[132:133] op_sel_hi:[1,0]
	s_waitcnt vmcnt(7)
	v_pk_mul_f32 v[146:147], v[166:167], v[134:135] op_sel_hi:[1,0]
	v_cvt_pk_f16_f32 v151, v144, v145
	v_pk_mul_f32 v[144:145], v[164:165], v[134:135] op_sel_hi:[1,0]
	v_add_co_u32_e32 v156, vcc, s0, v136
	v_cvt_pk_f16_f32 v144, v144, v145
	v_cvt_pk_f16_f32 v145, v146, v147
	v_pk_mul_f32 v[146:147], v[160:161], v[134:135] op_sel_hi:[1,0]
	v_pk_mul_f32 v[160:161], v[162:163], v[134:135] op_sel_hi:[1,0]
	v_addc_co_u32_e32 v157, vcc, 0, v137, vcc
	v_cvt_pk_f16_f32 v146, v146, v147
	v_cvt_pk_f16_f32 v147, v160, v161
	s_mov_b32 s0, 0x210000
	v_add_co_u32_e32 v196, vcc, s0, v136
	s_mov_b32 s0, 0x220000
	s_nop 0
	v_addc_co_u32_e32 v197, vcc, 0, v137, vcc
	global_load_dwordx4 v[156:159], v[156:157], off
	s_waitcnt vmcnt(5)
	v_cvt_pk_f16_f32 v163, v173, v177
	v_cvt_pk_f16_f32 v167, v172, v176
	s_waitcnt vmcnt(3)
	v_cvt_pk_f16_f32 v162, v185, v169
	s_waitcnt vmcnt(2)
	v_cvt_pk_f16_f32 v161, v189, v181
	s_waitcnt vmcnt(1)
	v_cvt_pk_f16_f32 v164, v152, v192
	v_add_co_u32_e32 v192, vcc, s0, v136
	v_cvt_pk_f16_f32 v160, v153, v193
	s_nop 0
	v_addc_co_u32_e32 v193, vcc, 0, v137, vcc
	s_mov_b32 s0, 0x230000
	v_cvt_pk_f16_f32 v166, v184, v168
	v_mfma_f32_32x32x16_f16 v[34:49], v[148:151], v[160:163], v[34:49]
	v_add_co_u32_e32 v184, vcc, s0, v136
	v_cvt_pk_f16_f32 v165, v188, v180
	s_nop 0
	v_addc_co_u32_e32 v185, vcc, 0, v137, vcc
	s_mov_b32 s0, 0x240000
	v_add_co_u32_e32 v188, vcc, s0, v136
	v_mfma_f32_32x32x16_f16 v[2:17], v[144:147], v[160:163], v[2:17]
	v_cvt_pk_f16_f32 v163, v174, v178
	v_cvt_pk_f16_f32 v162, v186, v170
	v_cvt_pk_f16_f32 v161, v190, v182
	v_cvt_pk_f16_f32 v160, v154, v194
	v_addc_co_u32_e32 v189, vcc, 0, v137, vcc
	s_mov_b32 s0, 0x250000
	v_mfma_f32_32x32x16_f16 v[114:129], v[148:151], v[160:163], v[114:129]
	v_add_co_u32_e32 v172, vcc, s0, v136
	s_mov_b32 s0, 0x260000
	s_nop 0
	v_addc_co_u32_e32 v173, vcc, 0, v137, vcc
	v_add_co_u32_e32 v176, vcc, s0, v136
	v_mfma_f32_32x32x16_f16 v[82:97], v[144:147], v[160:163], v[82:97]
	v_cvt_pk_f16_f32 v163, v175, v179
	v_cvt_pk_f16_f32 v162, v187, v171
	v_cvt_pk_f16_f32 v161, v191, v183
	v_cvt_pk_f16_f32 v160, v155, v195
	v_addc_co_u32_e32 v177, vcc, 0, v137, vcc
	s_mov_b32 s0, 0x270000
	v_mfma_f32_32x32x16_f16 v[98:113], v[148:151], v[164:167], v[98:113]
	v_add_co_u32_e32 v180, vcc, s0, v136
	s_mov_b32 s0, 0x300000
	s_nop 0
	v_addc_co_u32_e32 v181, vcc, 0, v137, vcc
	v_mfma_f32_32x32x16_f16 v[50:65], v[148:151], v[160:163], v[50:65]
	global_load_dwordx4 v[148:151], v[140:141], off offset:144
	global_load_dwordx4 v[152:155], v[140:141], off offset:128
	v_mfma_f32_32x32x16_f16 v[66:81], v[144:147], v[164:167], v[66:81]
	global_load_dwordx4 v[164:167], v[138:139], off offset:144
	global_load_dwordx4 v[168:171], v[138:139], off offset:128
	s_nop 0
	global_load_dwordx4 v[172:175], v[172:173], off
	s_nop 0
	global_load_dwordx4 v[176:179], v[176:177], off
	s_nop 0
	global_load_dwordx4 v[180:183], v[180:181], off
	s_nop 0
	global_load_dwordx4 v[184:187], v[184:185], off
	s_nop 0
	global_load_dwordx4 v[188:191], v[188:189], off
	s_nop 0
	global_load_dwordx4 v[192:195], v[192:193], off
	s_nop 0
	global_load_dwordx4 v[196:199], v[196:197], off
	v_mfma_f32_32x32x16_f16 v[18:33], v[144:147], v[160:163], v[18:33]
	s_waitcnt vmcnt(9)
	v_mul_f32_e64 v144, v152, v132
	v_mul_f32_e64 v145, v153, v132
	v_mul_f32_e64 v146, v154, v132
	v_mul_f32_e64 v147, v155, v132
	v_cvt_pk_f16_f32 v144, v144, v145
	v_cvt_pk_f16_f32 v145, v146, v147
	v_pk_mul_f32 v[146:147], v[148:149], v[132:133] op_sel_hi:[1,0]
	v_pk_mul_f32 v[148:149], v[150:151], v[132:133] op_sel_hi:[1,0]
	v_cvt_pk_f16_f32 v146, v146, v147
	v_cvt_pk_f16_f32 v147, v148, v149
	s_waitcnt vmcnt(7)
	v_pk_mul_f32 v[148:149], v[168:169], v[134:135] op_sel_hi:[1,0]
	v_pk_mul_f32 v[150:151], v[170:171], v[134:135] op_sel_hi:[1,0]
	v_cvt_pk_f16_f32 v148, v148, v149
	v_cvt_pk_f16_f32 v149, v150, v151
	v_pk_mul_f32 v[150:151], v[164:165], v[134:135] op_sel_hi:[1,0]
	v_pk_mul_f32 v[164:165], v[166:167], v[134:135] op_sel_hi:[1,0]
	v_cvt_pk_f16_f32 v150, v150, v151
	v_cvt_pk_f16_f32 v151, v164, v165
	v_add_co_u32_e32 v152, vcc, s0, v136
	s_mov_b32 s0, 0x310000
	s_nop 0
	v_addc_co_u32_e32 v153, vcc, 0, v137, vcc
	s_waitcnt vmcnt(4)
	v_cvt_pk_f16_f32 v163, v176, v180
	s_waitcnt vmcnt(2)
	v_cvt_pk_f16_f32 v162, v188, v172
	s_waitcnt vmcnt(1)
	v_cvt_pk_f16_f32 v161, v192, v184
	s_waitcnt vmcnt(0)
	v_cvt_pk_f16_f32 v160, v156, v196
	v_add_co_u32_e32 v196, vcc, s0, v136
	s_nop 0
	v_mfma_f32_32x32x16_f16 v[98:113], v[144:147], v[160:163], v[98:113]
	s_mov_b32 s0, 0x320000
	global_load_dwordx4 v[152:155], v[152:153], off
	v_mfma_f32_32x32x16_f16 v[66:81], v[148:151], v[160:163], v[66:81]
	v_cvt_pk_f16_f32 v160, v157, v197
	v_addc_co_u32_e32 v197, vcc, 0, v137, vcc
	v_add_co_u32_e32 v192, vcc, s0, v136
	v_cvt_pk_f16_f32 v163, v177, v181
	v_cvt_pk_f16_f32 v162, v189, v173
	v_cvt_pk_f16_f32 v161, v193, v185
	v_addc_co_u32_e32 v193, vcc, 0, v137, vcc
	s_mov_b32 s0, 0x330000
	v_mfma_f32_32x32x16_f16 v[34:49], v[144:147], v[160:163], v[34:49]
	v_add_co_u32_e32 v184, vcc, s0, v136
	s_mov_b32 s0, 0x340000
	s_nop 0
	v_addc_co_u32_e32 v185, vcc, 0, v137, vcc
	v_add_co_u32_e32 v188, vcc, s0, v136
	v_mfma_f32_32x32x16_f16 v[2:17], v[148:151], v[160:163], v[2:17]
	v_cvt_pk_f16_f32 v163, v178, v182
	v_cvt_pk_f16_f32 v162, v190, v174
	v_cvt_pk_f16_f32 v161, v194, v186
	v_cvt_pk_f16_f32 v160, v158, v198
	v_addc_co_u32_e32 v189, vcc, 0, v137, vcc
	s_mov_b32 s0, 0x350000
	v_mfma_f32_32x32x16_f16 v[114:129], v[144:147], v[160:163], v[114:129]
	v_add_co_u32_e32 v172, vcc, s0, v136
	s_mov_b32 s0, 0x360000
	s_nop 0
	v_addc_co_u32_e32 v173, vcc, 0, v137, vcc
	v_add_co_u32_e32 v176, vcc, s0, v136
	v_mfma_f32_32x32x16_f16 v[82:97], v[148:151], v[160:163], v[82:97]
	v_cvt_pk_f16_f32 v163, v179, v183
	v_cvt_pk_f16_f32 v162, v191, v175
	v_cvt_pk_f16_f32 v161, v195, v187
	v_cvt_pk_f16_f32 v160, v159, v199
	v_addc_co_u32_e32 v177, vcc, 0, v137, vcc
	s_mov_b32 s0, 0x370000
	v_mfma_f32_32x32x16_f16 v[50:65], v[144:147], v[160:163], v[50:65]
	global_load_dwordx4 v[144:147], v[140:141], off offset:208
	global_load_dwordx4 v[156:159], v[140:141], off offset:192
	global_load_dwordx4 v[164:167], v[138:139], off offset:208
	global_load_dwordx4 v[168:171], v[138:139], off offset:192
	v_add_co_u32_e32 v180, vcc, s0, v136
	global_load_dwordx4 v[172:175], v[172:173], off
	s_nop 0
	global_load_dwordx4 v[176:179], v[176:177], off
	v_addc_co_u32_e32 v181, vcc, 0, v137, vcc
	global_load_dwordx4 v[180:183], v[180:181], off
	s_nop 0
	global_load_dwordx4 v[184:187], v[184:185], off
	s_nop 0
	global_load_dwordx4 v[188:191], v[188:189], off
	s_nop 0
	global_load_dwordx4 v[192:195], v[192:193], off
	s_nop 0
	global_load_dwordx4 v[196:199], v[196:197], off
	v_mfma_f32_32x32x16_f16 v[18:33], v[148:151], v[160:163], v[18:33]
	s_mov_b32 s0, 0x400000
	s_waitcnt vmcnt(10)
	v_mul_f32_e64 v144, v144, v132
	v_mul_f32_e64 v145, v145, v132
	s_waitcnt vmcnt(9)
	v_pk_mul_f32 v[148:149], v[156:157], v[132:133] op_sel_hi:[1,0]
	v_pk_mul_f32 v[150:151], v[158:159], v[132:133] op_sel_hi:[1,0]
	v_cvt_pk_f16_f32 v148, v148, v149
	v_cvt_pk_f16_f32 v149, v150, v151
	v_cvt_pk_f16_f32 v150, v144, v145
	v_pk_mul_f32 v[144:145], v[146:147], v[132:133] op_sel_hi:[1,0]
	s_waitcnt vmcnt(7)
	v_pk_mul_f32 v[146:147], v[170:171], v[134:135] op_sel_hi:[1,0]
	v_cvt_pk_f16_f32 v151, v144, v145
	v_pk_mul_f32 v[144:145], v[168:169], v[134:135] op_sel_hi:[1,0]
	v_add_co_u32_e32 v156, vcc, s0, v136
	v_cvt_pk_f16_f32 v144, v144, v145
	v_cvt_pk_f16_f32 v145, v146, v147
	v_pk_mul_f32 v[146:147], v[164:165], v[134:135] op_sel_hi:[1,0]
	v_pk_mul_f32 v[164:165], v[166:167], v[134:135] op_sel_hi:[1,0]
	v_cvt_pk_f16_f32 v146, v146, v147
	v_cvt_pk_f16_f32 v147, v164, v165
	v_addc_co_u32_e32 v157, vcc, 0, v137, vcc
	s_mov_b32 s0, 0x410000
	s_waitcnt vmcnt(4)
	v_cvt_pk_f16_f32 v163, v176, v180
	s_waitcnt vmcnt(2)
	v_cvt_pk_f16_f32 v162, v188, v172
	s_waitcnt vmcnt(1)
	v_cvt_pk_f16_f32 v161, v192, v184
	s_waitcnt vmcnt(0)
	v_cvt_pk_f16_f32 v160, v152, v196
	v_add_co_u32_e32 v196, vcc, s0, v136
	s_nop 0
	v_mfma_f32_32x32x16_f16 v[98:113], v[148:151], v[160:163], v[98:113]
	s_mov_b32 s0, 0x420000
	global_load_dwordx4 v[156:159], v[156:157], off
	v_mfma_f32_32x32x16_f16 v[66:81], v[144:147], v[160:163], v[66:81]
	v_cvt_pk_f16_f32 v160, v153, v197
	v_addc_co_u32_e32 v197, vcc, 0, v137, vcc
	v_add_co_u32_e32 v192, vcc, s0, v136
	v_cvt_pk_f16_f32 v163, v177, v181
	v_cvt_pk_f16_f32 v162, v189, v173
	v_cvt_pk_f16_f32 v161, v193, v185
	v_addc_co_u32_e32 v193, vcc, 0, v137, vcc
	s_mov_b32 s0, 0x430000
	v_mfma_f32_32x32x16_f16 v[34:49], v[148:151], v[160:163], v[34:49]
	v_add_co_u32_e32 v184, vcc, s0, v136
	s_mov_b32 s0, 0x440000
	s_nop 0
	v_addc_co_u32_e32 v185, vcc, 0, v137, vcc
	v_add_co_u32_e32 v188, vcc, s0, v136
	v_mfma_f32_32x32x16_f16 v[2:17], v[144:147], v[160:163], v[2:17]
	v_cvt_pk_f16_f32 v163, v178, v182
	v_cvt_pk_f16_f32 v162, v190, v174
	v_cvt_pk_f16_f32 v161, v194, v186
	v_cvt_pk_f16_f32 v160, v154, v198
	v_addc_co_u32_e32 v189, vcc, 0, v137, vcc
	s_mov_b32 s0, 0x450000
	v_mfma_f32_32x32x16_f16 v[114:129], v[148:151], v[160:163], v[114:129]
	v_add_co_u32_e32 v172, vcc, s0, v136
	s_mov_b32 s0, 0x460000
	s_nop 0
	v_addc_co_u32_e32 v173, vcc, 0, v137, vcc
	v_add_co_u32_e32 v176, vcc, s0, v136
	v_mfma_f32_32x32x16_f16 v[82:97], v[144:147], v[160:163], v[82:97]
	v_cvt_pk_f16_f32 v163, v179, v183
	v_cvt_pk_f16_f32 v162, v191, v175
	v_cvt_pk_f16_f32 v161, v195, v187
	v_cvt_pk_f16_f32 v160, v155, v199
	v_addc_co_u32_e32 v177, vcc, 0, v137, vcc
	s_mov_b32 s0, 0x470000
	v_mfma_f32_32x32x16_f16 v[50:65], v[148:151], v[160:163], v[50:65]
	global_load_dwordx4 v[148:151], v[140:141], off offset:272
	global_load_dwordx4 v[152:155], v[140:141], off offset:256
	global_load_dwordx4 v[164:167], v[138:139], off offset:272
	global_load_dwordx4 v[168:171], v[138:139], off offset:256
	v_add_co_u32_e32 v180, vcc, s0, v136
	global_load_dwordx4 v[172:175], v[172:173], off
	s_nop 0
	global_load_dwordx4 v[176:179], v[176:177], off
	v_addc_co_u32_e32 v181, vcc, 0, v137, vcc
	global_load_dwordx4 v[180:183], v[180:181], off
	s_nop 0
	global_load_dwordx4 v[184:187], v[184:185], off
	s_nop 0
	global_load_dwordx4 v[188:191], v[188:189], off
	s_nop 0
	global_load_dwordx4 v[192:195], v[192:193], off
	s_nop 0
	global_load_dwordx4 v[196:199], v[196:197], off
	v_mfma_f32_32x32x16_f16 v[18:33], v[144:147], v[160:163], v[18:33]
	s_mov_b32 s0, 0x500000
	s_waitcnt vmcnt(9)
	v_mul_f32_e64 v144, v152, v132
	v_mul_f32_e64 v145, v153, v132
	v_mul_f32_e64 v146, v154, v132
	v_mul_f32_e64 v147, v155, v132
	v_cvt_pk_f16_f32 v144, v144, v145
	v_cvt_pk_f16_f32 v145, v146, v147
	v_pk_mul_f32 v[146:147], v[148:149], v[132:133] op_sel_hi:[1,0]
	v_pk_mul_f32 v[148:149], v[150:151], v[132:133] op_sel_hi:[1,0]
	v_cvt_pk_f16_f32 v146, v146, v147
	v_cvt_pk_f16_f32 v147, v148, v149
	s_waitcnt vmcnt(7)
	v_pk_mul_f32 v[148:149], v[168:169], v[134:135] op_sel_hi:[1,0]
	v_pk_mul_f32 v[150:151], v[170:171], v[134:135] op_sel_hi:[1,0]
	v_cvt_pk_f16_f32 v148, v148, v149
	v_cvt_pk_f16_f32 v149, v150, v151
	v_pk_mul_f32 v[150:151], v[164:165], v[134:135] op_sel_hi:[1,0]
	v_pk_mul_f32 v[164:165], v[166:167], v[134:135] op_sel_hi:[1,0]
	v_cvt_pk_f16_f32 v150, v150, v151
	v_cvt_pk_f16_f32 v151, v164, v165
	v_add_co_u32_e32 v152, vcc, s0, v136
	s_mov_b32 s0, 0x510000
	s_nop 0
	v_addc_co_u32_e32 v153, vcc, 0, v137, vcc
	s_waitcnt vmcnt(4)
	v_cvt_pk_f16_f32 v163, v176, v180
	s_waitcnt vmcnt(2)
	v_cvt_pk_f16_f32 v162, v188, v172
	s_waitcnt vmcnt(1)
	v_cvt_pk_f16_f32 v161, v192, v184
	s_waitcnt vmcnt(0)
	v_cvt_pk_f16_f32 v160, v156, v196
	v_add_co_u32_e32 v192, vcc, s0, v136
	s_nop 0
	v_mfma_f32_32x32x16_f16 v[98:113], v[144:147], v[160:163], v[98:113]
	s_mov_b32 s0, 0x520000
	global_load_dwordx4 v[152:155], v[152:153], off
	v_mfma_f32_32x32x16_f16 v[66:81], v[148:151], v[160:163], v[66:81]
	v_cvt_pk_f16_f32 v161, v193, v185
	v_addc_co_u32_e32 v193, vcc, 0, v137, vcc
	v_add_co_u32_e32 v188, vcc, s0, v136
	v_cvt_pk_f16_f32 v162, v189, v173
	s_nop 0
	v_addc_co_u32_e32 v189, vcc, 0, v137, vcc
	s_mov_b32 s0, 0x530000
	v_add_co_u32_e32 v180, vcc, s0, v136
	v_cvt_pk_f16_f32 v163, v177, v181
	v_cvt_pk_f16_f32 v160, v157, v197
	v_addc_co_u32_e32 v181, vcc, 0, v137, vcc
	s_mov_b32 s0, 0x540000
	v_mfma_f32_32x32x16_f16 v[34:49], v[144:147], v[160:163], v[34:49]
	v_add_co_u32_e32 v184, vcc, s0, v136
	s_mov_b32 s0, 0x550000
	s_nop 0
	v_addc_co_u32_e32 v185, vcc, 0, v137, vcc
	v_add_co_u32_e32 v164, vcc, s0, v136
	v_mfma_f32_32x32x16_f16 v[2:17], v[148:151], v[160:163], v[2:17]
	v_cvt_pk_f16_f32 v163, v178, v182
	v_cvt_pk_f16_f32 v162, v190, v174
	v_cvt_pk_f16_f32 v161, v194, v186
	v_cvt_pk_f16_f32 v160, v158, v198
	v_addc_co_u32_e32 v165, vcc, 0, v137, vcc
	s_mov_b32 s0, 0x560000
	v_mfma_f32_32x32x16_f16 v[114:129], v[144:147], v[160:163], v[114:129]
	v_mfma_f32_32x32x16_f16 v[82:97], v[148:151], v[160:163], v[82:97]
	v_cvt_pk_f16_f32 v163, v179, v183
	v_cvt_pk_f16_f32 v162, v191, v175
	v_cvt_pk_f16_f32 v161, v195, v187
	v_cvt_pk_f16_f32 v160, v159, v199
	s_nop 1
	v_mfma_f32_32x32x16_f16 v[50:65], v[144:147], v[160:163], v[50:65]
	global_load_dwordx4 v[144:147], v[140:141], off offset:336
	global_load_dwordx4 v[156:159], v[140:141], off offset:320
	v_add_co_u32_e32 v140, vcc, s0, v136
	s_mov_b32 s0, 0x570000
	s_nop 0
	v_addc_co_u32_e32 v141, vcc, 0, v137, vcc
	global_load_dwordx4 v[164:167], v[164:165], off
	s_nop 0
	global_load_dwordx4 v[168:171], v[140:141], off
	global_load_dwordx4 v[172:175], v[138:139], off offset:336
	s_nop 0
	global_load_dwordx4 v[138:141], v[138:139], off offset:320
	v_add_co_u32_e32 v136, vcc, s0, v136
	v_mfma_f32_32x32x16_f16 v[18:33], v[148:151], v[160:163], v[18:33]
	s_nop 0
	v_addc_co_u32_e32 v137, vcc, 0, v137, vcc
	global_load_dwordx4 v[176:179], v[136:137], off
	s_nop 0
	global_load_dwordx4 v[180:183], v[180:181], off
	s_nop 0
	global_load_dwordx4 v[184:187], v[184:185], off
	s_nop 0
	global_load_dwordx4 v[188:191], v[188:189], off
	s_nop 0
	global_load_dwordx4 v[192:195], v[192:193], off
	v_cmp_eq_u32_e32 vcc, 0, v135
	s_waitcnt vmcnt(9)
	v_pk_mul_f32 v[136:137], v[156:157], v[132:133] op_sel_hi:[1,0]
	s_nop 0
	v_cvt_pk_f16_f32 v148, v136, v137
	v_pk_mul_f32 v[136:137], v[158:159], v[132:133] op_sel_hi:[1,0]
	s_nop 0
	v_cvt_pk_f16_f32 v149, v136, v137
	v_pk_mul_f32 v[136:137], v[144:145], v[132:133] op_sel_hi:[1,0]
	s_waitcnt vmcnt(1)
	v_cvt_pk_f16_f32 v145, v188, v180
	v_cvt_pk_f16_f32 v150, v136, v137
	v_pk_mul_f32 v[136:137], v[146:147], v[132:133] op_sel_hi:[1,0]
	v_cvt_pk_f16_f32 v147, v168, v176
	v_cvt_pk_f16_f32 v151, v136, v137
	v_pk_mul_f32 v[136:137], v[138:139], v[134:135] op_sel_hi:[1,0]
	v_pk_mul_f32 v[138:139], v[140:141], v[134:135] op_sel_hi:[1,0]
	v_cvt_pk_f16_f32 v136, v136, v137
	v_cvt_pk_f16_f32 v137, v138, v139
	v_pk_mul_f32 v[138:139], v[172:173], v[134:135] op_sel_hi:[1,0]
	v_pk_mul_f32 v[140:141], v[174:175], v[134:135] op_sel_hi:[1,0]
	v_cvt_pk_f16_f32 v138, v138, v139
	v_cvt_pk_f16_f32 v139, v140, v141
	v_cvt_pk_f16_f32 v146, v184, v164
	s_waitcnt vmcnt(0)
	v_cvt_pk_f16_f32 v144, v152, v192
	v_and_b32_e32 v132, 63, v0
	v_lshlrev_b32_e32 v0, 2, v132
	v_mfma_f32_32x32x16_f16 v[98:113], v[148:151], v[144:147], v[98:113]
	v_lshl_or_b32 v140, v143, 15, v0
	v_lshlrev_b32_e32 v141, 14, v135
	v_or_b32_e32 v130, v140, v141
	v_mfma_f32_32x32x16_f16 v[66:81], v[136:139], v[144:147], v[66:81]
	v_cvt_pk_f16_f32 v147, v169, v177
	v_cvt_pk_f16_f32 v146, v185, v165
	v_cvt_pk_f16_f32 v145, v189, v181
	v_cvt_pk_f16_f32 v144, v153, v193
	s_nop 1
	v_mfma_f32_32x32x16_f16 v[34:49], v[148:151], v[144:147], v[34:49]
	v_mfma_f32_32x32x16_f16 v[2:17], v[136:139], v[144:147], v[2:17]
	v_cvt_pk_f16_f32 v147, v170, v178
	v_cvt_pk_f16_f32 v146, v186, v166
	v_cvt_pk_f16_f32 v145, v190, v182
	v_cvt_pk_f16_f32 v144, v154, v194
	s_nop 1
	v_mfma_f32_32x32x16_f16 v[114:129], v[148:151], v[144:147], v[114:129]
	v_mfma_f32_32x32x16_f16 v[82:97], v[136:139], v[144:147], v[82:97]
	s_nop 10
	s_cbranch_vccz .Lk1_role1
	ds_write2st64_b32 v130, v114, v115 offset1:1
	ds_write2st64_b32 v130, v116, v117 offset0:2 offset1:3
	ds_write2st64_b32 v130, v118, v119 offset0:4 offset1:5
	ds_write2st64_b32 v130, v120, v121 offset0:6 offset1:7
	ds_write2st64_b32 v130, v122, v123 offset0:8 offset1:9
	ds_write2st64_b32 v130, v124, v125 offset0:10 offset1:11
	v_cvt_pk_f16_f32 v147, v171, v179
	v_cvt_pk_f16_f32 v146, v187, v167
	v_cvt_pk_f16_f32 v145, v191, v183
	v_cvt_pk_f16_f32 v144, v155, v195
	ds_write2st64_b32 v130, v126, v127 offset0:12 offset1:13
	s_nop 1
	v_mfma_f32_32x32x16_f16 v[50:65], v[148:151], v[144:147], v[50:65]
	ds_write2st64_b32 v130, v128, v129 offset0:14 offset1:15
	ds_write2st64_b32 v130, v82, v83 offset0:16 offset1:17
	ds_write2st64_b32 v130, v84, v85 offset0:18 offset1:19
	ds_write2st64_b32 v130, v86, v87 offset0:20 offset1:21
	ds_write2st64_b32 v130, v88, v89 offset0:22 offset1:23
	ds_write2st64_b32 v130, v90, v91 offset0:24 offset1:25
	ds_write2st64_b32 v130, v92, v93 offset0:26 offset1:27
	ds_write2st64_b32 v130, v94, v95 offset0:28 offset1:29
	s_nop 1
	v_mfma_f32_32x32x16_f16 v[18:33], v[136:139], v[144:147], v[18:33]
	s_nop 11
	ds_write2st64_b32 v130, v96, v97 offset0:30 offset1:31
	ds_write2st64_b32 v130, v50, v51 offset0:32 offset1:33
	ds_write2st64_b32 v130, v52, v53 offset0:34 offset1:35
	ds_write2st64_b32 v130, v54, v55 offset0:36 offset1:37
	ds_write2st64_b32 v130, v56, v57 offset0:38 offset1:39
	ds_write2st64_b32 v130, v58, v59 offset0:40 offset1:41
	ds_write2st64_b32 v130, v60, v61 offset0:42 offset1:43
	ds_write2st64_b32 v130, v62, v63 offset0:44 offset1:45
	ds_write2st64_b32 v130, v64, v65 offset0:46 offset1:47
	ds_write2st64_b32 v130, v18, v19 offset0:48 offset1:49
	ds_write2st64_b32 v130, v20, v21 offset0:50 offset1:51
	ds_write2st64_b32 v130, v22, v23 offset0:52 offset1:53
	ds_write2st64_b32 v130, v24, v25 offset0:54 offset1:55
	ds_write2st64_b32 v130, v26, v27 offset0:56 offset1:57
	ds_write2st64_b32 v130, v28, v29 offset0:58 offset1:59
	ds_write2st64_b32 v130, v30, v31 offset0:60 offset1:61
	ds_write2st64_b32 v130, v32, v33 offset0:62 offset1:63
	v_lshlrev_b32_e32 v0, 2, v1
	v_lshl_or_b32 v143, v135, 1, v0
	v_mbcnt_lo_u32_b32 v0, -1, 0
	v_mbcnt_hi_u32_b32 v0, -1, v0
	v_and_b32_e32 v130, 64, v0
	v_xor_b32_e32 v1, 32, v0
	v_add_u32_e32 v130, 64, v130
	v_cmp_lt_i32_e64 s[0:1], v1, v130
	v_lshlrev_b32_e32 v130, 1, v142
	s_waitcnt lgkmcnt(0)
	v_cndmask_b32_e64 v0, v0, v1, s[0:1]
	v_lshlrev_b32_e32 v144, 2, v0
	v_xor_b32_e32 v0, 0x4000, v141
	v_or_b32_e32 v142, v140, v0
	s_barrier
	ds_read2st64_b32 v[0:1], v142 offset1:1
	ds_read2st64_b32 v[134:135], v142 offset0:4 offset1:5
	ds_read2st64_b32 v[136:137], v142 offset0:6 offset1:7
	ds_read2st64_b32 v[138:139], v142 offset0:2 offset1:3
	s_waitcnt lgkmcnt(3)
	v_add_f32_e32 v0, v98, v0
	s_waitcnt lgkmcnt(2)
	v_add_f32_e32 v98, v102, v134
	v_add_f32_e32 v1, v99, v1
	v_add_f32_e32 v99, v103, v135
	s_waitcnt lgkmcnt(0)
	v_add_f32_e32 v100, v100, v138
	v_add_f32_e32 v102, v104, v136
	v_add_f32_e32 v101, v101, v139
	v_cvt_pk_f16_f32 v104, v0, v1
	v_add_f32_e32 v0, v105, v137
	v_cvt_pk_f16_f32 v100, v100, v101
	v_cvt_pk_f16_f32 v101, v98, v99
	v_cvt_pk_f16_f32 v102, v102, v0
	v_cmp_gt_u32_e64 s[0:1], 32, v132
	v_mov_b32_e32 v120, 0x3c00
	v_bfrev_b32_e32 v121, 60
	s_nop 1
	v_permlane32_swap_b32_e32 v100, v102
	v_permlane32_swap_b32_e32 v104, v101
	s_nop 0
	v_lshlrev_b32_e32 v145, 7, v133
	s_waitcnt lgkmcnt(1)
	v_mov_b32_e32 v99, v100
	v_mov_b32_e32 v100, v102
	s_waitcnt lgkmcnt(0)
	v_mov_b32_e32 v102, v101
	v_cndmask_b32_e64 v103, v120, v102, s[0:1]
	v_cndmask_b32_e64 v101, v121, v100, s[0:1]
	v_mov_b32_e32 v98, v104
	v_bfi_b32 v101, s2, v100, v101
	v_bfi_b32 v100, s2, v103, v102
	ds_read2st64_b32 v[102:103], v142 offset0:8 offset1:9
	ds_read2st64_b32 v[104:105], v142 offset0:12 offset1:13
	ds_read2st64_b32 v[114:115], v142 offset0:14 offset1:15
	ds_read2st64_b32 v[116:117], v142 offset0:10 offset1:11
	v_or_b32_e32 v119, v143, v145
	v_lshl_add_u64 v[0:1], s[8:9], 0, v[130:131]
	s_waitcnt lgkmcnt(3)
	v_add_f32_e32 v102, v106, v102
	v_add_f32_e32 v103, v107, v103
	s_waitcnt lgkmcnt(2)
	v_add_f32_e32 v105, v111, v105
	v_add_f32_e32 v104, v110, v104
	s_waitcnt lgkmcnt(0)
	v_add_f32_e32 v106, v108, v116
	v_add_f32_e32 v107, v112, v114
	v_add_f32_e32 v108, v109, v117
	v_cvt_pk_f16_f32 v110, v102, v103
	v_add_f32_e32 v102, v113, v115
	v_cvt_pk_f16_f32 v106, v106, v108
	v_cvt_pk_f16_f32 v104, v104, v105
	v_cvt_pk_f16_f32 v105, v107, v102
	s_nop 1
	v_permlane32_swap_b32_e32 v106, v105
	v_permlane32_swap_b32_e32 v110, v104
	s_nop 0
	v_add_u32_e32 v130, s3, v119
	v_lshlrev_b64 v[102:103], 5, v[130:131]
	v_lshl_add_u64 v[102:103], v[0:1], 0, v[102:103]
	global_store_dwordx4 v[102:103], v[98:101], off
	s_waitcnt lgkmcnt(0)
	v_mov_b32_e32 v102, v104
	v_mov_b32_e32 v100, v105
	v_xor_b32_e32 v82, 0x5000, v141
	v_mov_b32_e32 v98, v110
	v_cndmask_b32_e64 v103, v120, v102, s[0:1]
	v_cndmask_b32_e64 v101, v121, v100, s[0:1]
	v_or_b32_e32 v110, v140, v82
	v_mov_b32_e32 v99, v106
	v_bfi_b32 v101, s2, v100, v101
	v_bfi_b32 v100, s2, v103, v102
	ds_read2st64_b32 v[102:103], v110 offset1:1
	ds_read2st64_b32 v[104:105], v110 offset0:4 offset1:5
	ds_read2st64_b32 v[106:107], v110 offset0:6 offset1:7
	ds_read2st64_b32 v[108:109], v110 offset0:2 offset1:3
	s_waitcnt lgkmcnt(3)
	v_add_f32_e32 v66, v66, v102
	v_add_f32_e32 v67, v67, v103
	s_waitcnt lgkmcnt(2)
	v_add_f32_e32 v70, v70, v104
	v_add_f32_e32 v71, v71, v105
	s_waitcnt lgkmcnt(0)
	v_add_f32_e32 v68, v68, v108
	v_add_f32_e32 v72, v72, v106
	v_add_f32_e32 v69, v69, v109
	v_cvt_pk_f16_f32 v82, v66, v67
	v_add_f32_e32 v66, v73, v107
	v_cvt_pk_f16_f32 v68, v68, v69
	v_cvt_pk_f16_f32 v69, v70, v71
	v_cvt_pk_f16_f32 v70, v72, v66
	s_nop 1
	v_permlane32_swap_b32_e32 v68, v70
	v_permlane32_swap_b32_e32 v82, v69
	s_nop 0
	v_lshl_add_u32 v118, v143, 7, v133
	v_add_u32_e32 v130, s4, v118
	v_lshlrev_b64 v[66:67], 5, v[130:131]
	v_lshl_add_u64 v[66:67], v[0:1], 0, v[66:67]
	global_store_dwordx4 v[66:67], v[98:101], off
	s_waitcnt lgkmcnt(1)
	v_mov_b32_e32 v67, v68
	v_mov_b32_e32 v68, v70
	s_waitcnt lgkmcnt(0)
	v_mov_b32_e32 v70, v69
	v_cndmask_b32_e64 v71, v120, v70, s[0:1]
	v_cndmask_b32_e64 v69, v121, v68, s[0:1]
	v_mov_b32_e32 v66, v82
	v_bfi_b32 v69, s2, v68, v69
	v_bfi_b32 v68, s2, v71, v70
	ds_read2st64_b32 v[70:71], v110 offset0:8 offset1:9
	ds_read2st64_b32 v[72:73], v110 offset0:12 offset1:13
	ds_read2st64_b32 v[82:83], v110 offset0:14 offset1:15
	ds_read2st64_b32 v[84:85], v110 offset0:10 offset1:11
	s_waitcnt lgkmcnt(3)
	v_add_f32_e32 v70, v74, v70
	v_add_f32_e32 v71, v75, v71
	s_waitcnt lgkmcnt(2)
	v_add_f32_e32 v73, v79, v73
	v_add_f32_e32 v72, v78, v72
	s_waitcnt lgkmcnt(0)
	v_add_f32_e32 v74, v76, v84
	v_add_f32_e32 v75, v80, v82
	v_add_f32_e32 v76, v77, v85
	v_cvt_pk_f16_f32 v78, v70, v71
	v_add_f32_e32 v70, v81, v83
	v_cvt_pk_f16_f32 v74, v74, v76
	v_cvt_pk_f16_f32 v72, v72, v73
	v_cvt_pk_f16_f32 v73, v75, v70
	s_nop 1
	v_permlane32_swap_b32_e32 v74, v73
	v_permlane32_swap_b32_e32 v78, v72
	s_nop 0
	v_add_u32_e32 v130, s5, v119
	v_lshlrev_b64 v[70:71], 5, v[130:131]
	v_lshl_add_u64 v[70:71], v[0:1], 0, v[70:71]
	global_store_dwordx4 v[70:71], v[66:69], off
	s_waitcnt lgkmcnt(0)
	v_mov_b32_e32 v70, v72
	v_cndmask_b32_e64 v71, v120, v70, s[0:1]
	v_mov_b32_e32 v68, v73
	v_cndmask_b32_e64 v69, v121, v68, s[0:1]
	v_add_u32_e32 v130, s6, v118
	v_bfi_b32 v69, s2, v68, v69
	v_bfi_b32 v68, s2, v71, v70
	v_lshlrev_b64 v[70:71], 5, v[130:131]
	v_mov_b32_e32 v67, v74
	v_mov_b32_e32 v66, v78
	v_lshl_add_u64 v[70:71], v[0:1], 0, v[70:71]
	v_xor_b32_e32 v50, 0x6000, v141
	global_store_dwordx4 v[70:71], v[66:69], off
	v_or_b32_e32 v74, v140, v50
	ds_read2st64_b32 v[66:67], v74 offset1:1
	ds_read2st64_b32 v[68:69], v74 offset0:4 offset1:5
	ds_read2st64_b32 v[70:71], v74 offset0:6 offset1:7
	ds_read2st64_b32 v[72:73], v74 offset0:2 offset1:3
	s_waitcnt lgkmcnt(3)
	v_add_f32_e32 v34, v34, v66
	v_add_f32_e32 v35, v35, v67
	s_waitcnt lgkmcnt(0)
	v_add_f32_e32 v36, v36, v72
	v_add_f32_e32 v37, v37, v73
	v_add_f32_e32 v38, v38, v68
	v_add_f32_e32 v39, v39, v69
	v_add_f32_e32 v40, v40, v70
	v_cvt_pk_f16_f32 v34, v34, v35
	v_cvt_pk_f16_f32 v35, v36, v37
	v_add_f32_e32 v36, v41, v71
	v_cvt_pk_f16_f32 v37, v38, v39
	v_cvt_pk_f16_f32 v36, v40, v36
	s_nop 1
	v_permlane32_swap_b32_e32 v35, v36
	v_permlane32_swap_b32_e32 v34, v37
	s_nop 0
	v_or_b32_e32 v40, 1, v143
	v_lshl_add_u32 v54, v40, 7, v133
	v_or_b32_e32 v55, v40, v145
	s_waitcnt lgkmcnt(1)
	s_nop 0
	s_nop 0
	s_waitcnt lgkmcnt(0)
	v_mov_b32_e32 v38, v37
	s_nop 0
	v_cndmask_b32_e64 v39, v120, v38, s[0:1]
	v_cndmask_b32_e64 v37, v121, v36, s[0:1]
	v_bfi_b32 v37, s2, v36, v37
	v_bfi_b32 v36, s2, v39, v38
	ds_read2st64_b32 v[38:39], v74 offset0:8 offset1:9
	ds_read2st64_b32 v[40:41], v74 offset0:12 offset1:13
	ds_read2st64_b32 v[50:51], v74 offset0:14 offset1:15
	ds_read2st64_b32 v[52:53], v74 offset0:10 offset1:11
	s_waitcnt lgkmcnt(3)
	v_add_f32_e32 v38, v42, v38
	v_add_f32_e32 v39, v43, v39
	s_waitcnt lgkmcnt(2)
	v_add_f32_e32 v41, v47, v41
	v_add_f32_e32 v40, v46, v40
	s_waitcnt lgkmcnt(0)
	v_add_f32_e32 v42, v44, v52
	v_add_f32_e32 v43, v48, v50
	v_add_f32_e32 v44, v45, v53
	v_cvt_pk_f16_f32 v46, v38, v39
	v_add_f32_e32 v38, v49, v51
	v_cvt_pk_f16_f32 v42, v42, v44
	v_cvt_pk_f16_f32 v40, v40, v41
	v_cvt_pk_f16_f32 v41, v43, v38
	s_nop 1
	v_permlane32_swap_b32_e32 v42, v41
	v_permlane32_swap_b32_e32 v46, v40
	s_nop 0
	v_add_u32_e32 v130, s3, v55
	v_lshlrev_b64 v[38:39], 5, v[130:131]
	v_lshl_add_u64 v[38:39], v[0:1], 0, v[38:39]
	global_store_dwordx4 v[38:39], v[34:37], off
	s_waitcnt lgkmcnt(0)
	v_mov_b32_e32 v38, v40
	v_mov_b32_e32 v36, v41
	v_xor_b32_e32 v18, 0x7000, v141
	v_cndmask_b32_e64 v39, v120, v38, s[0:1]
	v_cndmask_b32_e64 v37, v121, v36, s[0:1]
	v_or_b32_e32 v18, v140, v18
	v_mov_b32_e32 v35, v42
	v_mov_b32_e32 v34, v46
	v_bfi_b32 v37, s2, v36, v37
	v_bfi_b32 v36, s2, v39, v38
	ds_read2st64_b32 v[38:39], v18 offset1:1
	ds_read2st64_b32 v[40:41], v18 offset0:4 offset1:5
	ds_read2st64_b32 v[42:43], v18 offset0:6 offset1:7
	ds_read2st64_b32 v[44:45], v18 offset0:2 offset1:3
	s_waitcnt lgkmcnt(3)
	v_add_f32_e32 v2, v2, v38
	v_add_f32_e32 v3, v3, v39
	s_waitcnt lgkmcnt(2)
	v_add_f32_e32 v6, v6, v40
	v_add_f32_e32 v7, v7, v41
	s_waitcnt lgkmcnt(0)
	v_add_f32_e32 v4, v4, v44
	v_add_f32_e32 v8, v8, v42
	v_add_f32_e32 v5, v5, v45
	v_cvt_pk_f16_f32 v19, v2, v3
	v_add_f32_e32 v2, v9, v43
	v_cvt_pk_f16_f32 v4, v4, v5
	v_cvt_pk_f16_f32 v5, v6, v7
	v_cvt_pk_f16_f32 v6, v8, v2
	s_nop 1
	v_permlane32_swap_b32_e32 v4, v6
	v_permlane32_swap_b32_e32 v19, v5
	s_nop 0
	v_add_u32_e32 v130, s4, v54
	v_lshlrev_b64 v[2:3], 5, v[130:131]
	v_lshl_add_u64 v[2:3], v[0:1], 0, v[2:3]
	global_store_dwordx4 v[2:3], v[34:37], off
	s_waitcnt lgkmcnt(1)
	v_mov_b32_e32 v3, v4
	v_mov_b32_e32 v4, v6
	s_waitcnt lgkmcnt(0)
	v_mov_b32_e32 v6, v5
	v_cndmask_b32_e64 v7, v120, v6, s[0:1]
	v_cndmask_b32_e64 v5, v121, v4, s[0:1]
	v_mov_b32_e32 v2, v19
	v_bfi_b32 v5, s2, v4, v5
	v_bfi_b32 v4, s2, v7, v6
	ds_read2st64_b32 v[6:7], v18 offset0:8 offset1:9
	ds_read2st64_b32 v[8:9], v18 offset0:12 offset1:13
	v_mov_b32_e32 v19, v10
	v_mov_b32_e32 v21, v11
	ds_read2st64_b32 v[10:11], v18 offset0:14 offset1:15
	v_mov_b32_e32 v20, v14
	v_mov_b32_e32 v22, v15
	ds_read2st64_b32 v[14:15], v18 offset0:10 offset1:11
	s_waitcnt lgkmcnt(3)
	v_add_f32_e32 v6, v19, v6
	v_add_f32_e32 v7, v21, v7
	s_waitcnt lgkmcnt(2)
	v_add_f32_e32 v8, v20, v8
	v_add_f32_e32 v9, v22, v9
	s_waitcnt lgkmcnt(1)
	v_add_f32_e32 v10, v16, v10
	s_waitcnt lgkmcnt(0)
	v_add_f32_e32 v12, v12, v14
	v_add_f32_e32 v13, v13, v15
	v_cvt_pk_f16_f32 v14, v6, v7
	v_add_f32_e32 v6, v17, v11
	v_cvt_pk_f16_f32 v12, v12, v13
	v_cvt_pk_f16_f32 v8, v8, v9
	v_cvt_pk_f16_f32 v9, v10, v6
	s_nop 1
	v_permlane32_swap_b32_e32 v12, v9
	v_permlane32_swap_b32_e32 v14, v8
	s_nop 0
	v_add_u32_e32 v130, s5, v55
	v_lshlrev_b64 v[6:7], 5, v[130:131]
	v_lshl_add_u64 v[6:7], v[0:1], 0, v[6:7]
	global_store_dwordx4 v[6:7], v[2:5], off
	s_waitcnt lgkmcnt(0)
	v_mov_b32_e32 v6, v8
	v_cndmask_b32_e64 v7, v120, v6, s[0:1]
	v_mov_b32_e32 v4, v9
	v_cndmask_b32_e64 v5, v121, v4, s[0:1]
	v_add_u32_e32 v130, s6, v54
	v_bfi_b32 v5, s2, v4, v5
	v_bfi_b32 v4, s2, v7, v6
	v_lshlrev_b64 v[6:7], 5, v[130:131]
	v_mov_b32_e32 v3, v12
	v_mov_b32_e32 v2, v14
	v_lshl_add_u64 v[0:1], v[0:1], 0, v[6:7]
	global_store_dwordx4 v[0:1], v[2:5], off
	s_endpgm
.Lk1_role1:
	ds_write2st64_b32 v130, v98, v99 offset1:1
	ds_write2st64_b32 v130, v100, v101 offset0:2 offset1:3
	ds_write2st64_b32 v130, v102, v103 offset0:4 offset1:5
	ds_write2st64_b32 v130, v104, v105 offset0:6 offset1:7
	ds_write2st64_b32 v130, v106, v107 offset0:8 offset1:9
	ds_write2st64_b32 v130, v108, v109 offset0:10 offset1:11
	v_cvt_pk_f16_f32 v147, v171, v179
	v_cvt_pk_f16_f32 v146, v187, v167
	v_cvt_pk_f16_f32 v145, v191, v183
	v_cvt_pk_f16_f32 v144, v155, v195
	ds_write2st64_b32 v130, v110, v111 offset0:12 offset1:13
	s_nop 1
	v_mfma_f32_32x32x16_f16 v[50:65], v[148:151], v[144:147], v[50:65]
	ds_write2st64_b32 v130, v112, v113 offset0:14 offset1:15
	ds_write2st64_b32 v130, v66, v67 offset0:16 offset1:17
	ds_write2st64_b32 v130, v68, v69 offset0:18 offset1:19
	ds_write2st64_b32 v130, v70, v71 offset0:20 offset1:21
	ds_write2st64_b32 v130, v72, v73 offset0:22 offset1:23
	ds_write2st64_b32 v130, v74, v75 offset0:24 offset1:25
	ds_write2st64_b32 v130, v76, v77 offset0:26 offset1:27
	ds_write2st64_b32 v130, v78, v79 offset0:28 offset1:29
	s_nop 1
	v_mfma_f32_32x32x16_f16 v[18:33], v[136:139], v[144:147], v[18:33]
	s_nop 11
	ds_write2st64_b32 v130, v80, v81 offset0:30 offset1:31
	ds_write2st64_b32 v130, v34, v35 offset0:32 offset1:33
	ds_write2st64_b32 v130, v36, v37 offset0:34 offset1:35
	ds_write2st64_b32 v130, v38, v39 offset0:36 offset1:37
	ds_write2st64_b32 v130, v40, v41 offset0:38 offset1:39
	ds_write2st64_b32 v130, v42, v43 offset0:40 offset1:41
	ds_write2st64_b32 v130, v44, v45 offset0:42 offset1:43
	ds_write2st64_b32 v130, v46, v47 offset0:44 offset1:45
	ds_write2st64_b32 v130, v48, v49 offset0:46 offset1:47
	ds_write2st64_b32 v130, v2, v3 offset0:48 offset1:49
	ds_write2st64_b32 v130, v4, v5 offset0:50 offset1:51
	ds_write2st64_b32 v130, v6, v7 offset0:52 offset1:53
	ds_write2st64_b32 v130, v8, v9 offset0:54 offset1:55
	ds_write2st64_b32 v130, v10, v11 offset0:56 offset1:57
	ds_write2st64_b32 v130, v12, v13 offset0:58 offset1:59
	ds_write2st64_b32 v130, v14, v15 offset0:60 offset1:61
	ds_write2st64_b32 v130, v16, v17 offset0:62 offset1:63
	v_lshlrev_b32_e32 v0, 2, v1
	v_lshl_or_b32 v143, v135, 1, v0
	v_mbcnt_lo_u32_b32 v0, -1, 0
	v_mbcnt_hi_u32_b32 v0, -1, v0
	v_and_b32_e32 v130, 64, v0
	v_xor_b32_e32 v1, 32, v0
	v_add_u32_e32 v130, 64, v130
	v_cmp_lt_i32_e64 s[0:1], v1, v130
	v_lshlrev_b32_e32 v130, 1, v142
	s_waitcnt lgkmcnt(0)
	v_cndmask_b32_e64 v0, v0, v1, s[0:1]
	v_lshlrev_b32_e32 v144, 2, v0
	v_xor_b32_e32 v0, 0x4000, v141
	v_or_b32_e32 v142, v140, v0
	s_barrier
	ds_read2st64_b32 v[0:1], v142 offset1:1
	ds_read2st64_b32 v[134:135], v142 offset0:4 offset1:5
	ds_read2st64_b32 v[136:137], v142 offset0:6 offset1:7
	ds_read2st64_b32 v[138:139], v142 offset0:2 offset1:3
	s_waitcnt lgkmcnt(3)
	v_add_f32_e32 v0, v114, v0
	s_waitcnt lgkmcnt(2)
	v_add_f32_e32 v98, v118, v134
	v_add_f32_e32 v1, v115, v1
	v_add_f32_e32 v99, v119, v135
	s_waitcnt lgkmcnt(0)
	v_add_f32_e32 v100, v116, v138
	v_add_f32_e32 v102, v120, v136
	v_add_f32_e32 v101, v117, v139
	v_cvt_pk_f16_f32 v104, v0, v1
	v_add_f32_e32 v0, v121, v137
	v_cvt_pk_f16_f32 v100, v100, v101
	v_cvt_pk_f16_f32 v101, v98, v99
	v_cvt_pk_f16_f32 v102, v102, v0
	v_cmp_gt_u32_e64 s[0:1], 32, v132
	v_mov_b32_e32 v120, 0x3c00
	v_mov_b32_e32 v103, v121
	v_bfrev_b32_e32 v121, 60
	s_nop 1
	v_permlane32_swap_b32_e32 v100, v102
	v_permlane32_swap_b32_e32 v104, v101
	s_nop 0
	v_lshlrev_b32_e32 v145, 7, v133
	s_waitcnt lgkmcnt(1)
	v_mov_b32_e32 v99, v100
	v_mov_b32_e32 v100, v102
	s_waitcnt lgkmcnt(0)
	v_mov_b32_e32 v102, v101
	v_cndmask_b32_e64 v103, v120, v102, s[0:1]
	v_cndmask_b32_e64 v101, v121, v100, s[0:1]
	v_mov_b32_e32 v98, v104
	v_bfi_b32 v101, s2, v100, v101
	v_bfi_b32 v100, s2, v103, v102
	ds_read2st64_b32 v[102:103], v142 offset0:8 offset1:9
	ds_read2st64_b32 v[104:105], v142 offset0:12 offset1:13
	ds_read2st64_b32 v[114:115], v142 offset0:14 offset1:15
	ds_read2st64_b32 v[116:117], v142 offset0:10 offset1:11
	v_or_b32_e32 v119, v143, v145
	v_lshl_add_u64 v[0:1], s[8:9], 0, v[130:131]
	s_waitcnt lgkmcnt(3)
	v_add_f32_e32 v102, v122, v102
	v_add_f32_e32 v103, v123, v103
	s_waitcnt lgkmcnt(2)
	v_add_f32_e32 v105, v127, v105
	v_add_f32_e32 v104, v126, v104
	s_waitcnt lgkmcnt(0)
	v_add_f32_e32 v106, v124, v116
	v_add_f32_e32 v107, v128, v114
	v_add_f32_e32 v108, v125, v117
	v_cvt_pk_f16_f32 v110, v102, v103
	v_add_f32_e32 v102, v129, v115
	v_cvt_pk_f16_f32 v106, v106, v108
	v_cvt_pk_f16_f32 v104, v104, v105
	v_cvt_pk_f16_f32 v105, v107, v102
	s_nop 1
	v_permlane32_swap_b32_e32 v106, v105
	v_permlane32_swap_b32_e32 v110, v104
	s_nop 0
	v_add_u32_e32 v130, s3, v119
	v_lshlrev_b64 v[102:103], 5, v[130:131]
	v_lshl_add_u64 v[102:103], v[0:1], 0, v[102:103]
	global_store_dwordx4 v[102:103], v[98:101], off
	s_waitcnt lgkmcnt(0)
	v_mov_b32_e32 v102, v104
	v_mov_b32_e32 v100, v105
	v_mov_b32_e32 v66, v82
	v_xor_b32_e32 v82, 0x5000, v141
	v_mov_b32_e32 v98, v110
	v_cndmask_b32_e64 v103, v120, v102, s[0:1]
	v_cndmask_b32_e64 v101, v121, v100, s[0:1]
	v_or_b32_e32 v110, v140, v82
	v_mov_b32_e32 v99, v106
	v_bfi_b32 v101, s2, v100, v101
	v_bfi_b32 v100, s2, v103, v102
	ds_read2st64_b32 v[102:103], v110 offset1:1
	ds_read2st64_b32 v[104:105], v110 offset0:4 offset1:5
	ds_read2st64_b32 v[106:107], v110 offset0:6 offset1:7
	ds_read2st64_b32 v[108:109], v110 offset0:2 offset1:3
	s_waitcnt lgkmcnt(3)
	v_add_f32_e32 v66, v66, v102
	v_add_f32_e32 v67, v83, v103
	s_waitcnt lgkmcnt(2)
	v_add_f32_e32 v70, v86, v104
	v_add_f32_e32 v71, v87, v105
	s_waitcnt lgkmcnt(0)
	v_add_f32_e32 v68, v84, v108
	v_add_f32_e32 v72, v88, v106
	v_add_f32_e32 v69, v85, v109
	v_cvt_pk_f16_f32 v82, v66, v67
	v_add_f32_e32 v66, v89, v107
	v_cvt_pk_f16_f32 v68, v68, v69
	v_cvt_pk_f16_f32 v69, v70, v71
	v_cvt_pk_f16_f32 v70, v72, v66
	s_nop 1
	v_permlane32_swap_b32_e32 v68, v70
	v_permlane32_swap_b32_e32 v82, v69
	s_nop 0
	v_lshl_add_u32 v118, v143, 7, v133
	v_add_u32_e32 v130, s4, v118
	v_lshlrev_b64 v[66:67], 5, v[130:131]
	v_lshl_add_u64 v[66:67], v[0:1], 0, v[66:67]
	global_store_dwordx4 v[66:67], v[98:101], off
	s_waitcnt lgkmcnt(1)
	v_mov_b32_e32 v67, v68
	v_mov_b32_e32 v68, v70
	s_waitcnt lgkmcnt(0)
	v_mov_b32_e32 v70, v69
	v_cndmask_b32_e64 v71, v120, v70, s[0:1]
	v_cndmask_b32_e64 v69, v121, v68, s[0:1]
	v_mov_b32_e32 v66, v82
	v_bfi_b32 v69, s2, v68, v69
	v_bfi_b32 v68, s2, v71, v70
	ds_read2st64_b32 v[70:71], v110 offset0:8 offset1:9
	ds_read2st64_b32 v[72:73], v110 offset0:12 offset1:13
	ds_read2st64_b32 v[82:83], v110 offset0:14 offset1:15
	ds_read2st64_b32 v[84:85], v110 offset0:10 offset1:11
	s_waitcnt lgkmcnt(3)
	v_add_f32_e32 v70, v90, v70
	v_add_f32_e32 v71, v91, v71
	s_waitcnt lgkmcnt(2)
	v_add_f32_e32 v73, v95, v73
	v_add_f32_e32 v72, v94, v72
	s_waitcnt lgkmcnt(0)
	v_add_f32_e32 v74, v92, v84
	v_add_f32_e32 v75, v96, v82
	v_add_f32_e32 v76, v93, v85
	v_cvt_pk_f16_f32 v78, v70, v71
	v_add_f32_e32 v70, v97, v83
	v_cvt_pk_f16_f32 v74, v74, v76
	v_cvt_pk_f16_f32 v72, v72, v73
	v_cvt_pk_f16_f32 v73, v75, v70
	s_nop 1
	v_permlane32_swap_b32_e32 v74, v73
	v_permlane32_swap_b32_e32 v78, v72
	s_nop 0
	v_add_u32_e32 v130, s5, v119
	v_lshlrev_b64 v[70:71], 5, v[130:131]
	v_lshl_add_u64 v[70:71], v[0:1], 0, v[70:71]
	global_store_dwordx4 v[70:71], v[66:69], off
	s_waitcnt lgkmcnt(0)
	v_mov_b32_e32 v70, v72
	v_cndmask_b32_e64 v71, v120, v70, s[0:1]
	v_mov_b32_e32 v68, v73
	v_cndmask_b32_e64 v69, v121, v68, s[0:1]
	v_add_u32_e32 v130, s6, v118
	v_bfi_b32 v69, s2, v68, v69
	v_bfi_b32 v68, s2, v71, v70
	v_lshlrev_b64 v[70:71], 5, v[130:131]
	v_mov_b32_e32 v67, v74
	v_mov_b32_e32 v66, v78
	v_lshl_add_u64 v[70:71], v[0:1], 0, v[70:71]
	v_mov_b32_e32 v34, v50
	v_xor_b32_e32 v50, 0x6000, v141
	global_store_dwordx4 v[70:71], v[66:69], off
	v_or_b32_e32 v74, v140, v50
	ds_read2st64_b32 v[66:67], v74 offset1:1
	ds_read2st64_b32 v[68:69], v74 offset0:4 offset1:5
	ds_read2st64_b32 v[70:71], v74 offset0:6 offset1:7
	ds_read2st64_b32 v[72:73], v74 offset0:2 offset1:3
	s_waitcnt lgkmcnt(3)
	v_add_f32_e32 v34, v34, v66
	v_add_f32_e32 v35, v51, v67
	s_waitcnt lgkmcnt(0)
	v_add_f32_e32 v36, v52, v72
	v_add_f32_e32 v37, v53, v73
	v_add_f32_e32 v38, v54, v68
	v_add_f32_e32 v39, v55, v69
	v_add_f32_e32 v40, v56, v70
	v_cvt_pk_f16_f32 v34, v34, v35
	v_cvt_pk_f16_f32 v35, v36, v37
	v_add_f32_e32 v36, v57, v71
	v_cvt_pk_f16_f32 v37, v38, v39
	v_cvt_pk_f16_f32 v36, v40, v36
	s_nop 1
	v_permlane32_swap_b32_e32 v35, v36
	v_permlane32_swap_b32_e32 v34, v37
	s_nop 0
	v_or_b32_e32 v40, 1, v143
	v_lshl_add_u32 v54, v40, 7, v133
	v_or_b32_e32 v55, v40, v145
	s_waitcnt lgkmcnt(1)
	s_nop 0
	s_nop 0
	s_waitcnt lgkmcnt(0)
	v_mov_b32_e32 v38, v37
	s_nop 0
	v_cndmask_b32_e64 v39, v120, v38, s[0:1]
	v_cndmask_b32_e64 v37, v121, v36, s[0:1]
	v_bfi_b32 v37, s2, v36, v37
	v_bfi_b32 v36, s2, v39, v38
	ds_read2st64_b32 v[38:39], v74 offset0:8 offset1:9
	ds_read2st64_b32 v[40:41], v74 offset0:12 offset1:13
	ds_read2st64_b32 v[50:51], v74 offset0:14 offset1:15
	ds_read2st64_b32 v[52:53], v74 offset0:10 offset1:11
	s_waitcnt lgkmcnt(3)
	v_add_f32_e32 v38, v58, v38
	v_add_f32_e32 v39, v59, v39
	s_waitcnt lgkmcnt(2)
	v_add_f32_e32 v41, v63, v41
	v_add_f32_e32 v40, v62, v40
	s_waitcnt lgkmcnt(0)
	v_add_f32_e32 v42, v60, v52
	v_add_f32_e32 v43, v64, v50
	v_add_f32_e32 v44, v61, v53
	v_cvt_pk_f16_f32 v46, v38, v39
	v_add_f32_e32 v38, v65, v51
	v_cvt_pk_f16_f32 v42, v42, v44
	v_cvt_pk_f16_f32 v40, v40, v41
	v_cvt_pk_f16_f32 v41, v43, v38
	s_nop 1
	v_permlane32_swap_b32_e32 v42, v41
	v_permlane32_swap_b32_e32 v46, v40
	s_nop 0
	v_add_u32_e32 v130, s3, v55
	v_lshlrev_b64 v[38:39], 5, v[130:131]
	v_lshl_add_u64 v[38:39], v[0:1], 0, v[38:39]
	global_store_dwordx4 v[38:39], v[34:37], off
	s_waitcnt lgkmcnt(0)
	v_mov_b32_e32 v38, v40
	v_mov_b32_e32 v36, v41
	v_mov_b32_e32 v2, v18
	v_xor_b32_e32 v18, 0x7000, v141
	v_cndmask_b32_e64 v39, v120, v38, s[0:1]
	v_cndmask_b32_e64 v37, v121, v36, s[0:1]
	v_or_b32_e32 v18, v140, v18
	v_mov_b32_e32 v35, v42
	v_mov_b32_e32 v34, v46
	v_bfi_b32 v37, s2, v36, v37
	v_bfi_b32 v36, s2, v39, v38
	ds_read2st64_b32 v[38:39], v18 offset1:1
	ds_read2st64_b32 v[40:41], v18 offset0:4 offset1:5
	ds_read2st64_b32 v[42:43], v18 offset0:6 offset1:7
	ds_read2st64_b32 v[44:45], v18 offset0:2 offset1:3
	s_waitcnt lgkmcnt(3)
	v_add_f32_e32 v2, v2, v38
	v_add_f32_e32 v3, v19, v39
	s_waitcnt lgkmcnt(2)
	v_add_f32_e32 v6, v22, v40
	v_add_f32_e32 v7, v23, v41
	s_waitcnt lgkmcnt(0)
	v_add_f32_e32 v4, v20, v44
	v_add_f32_e32 v8, v24, v42
	v_add_f32_e32 v5, v21, v45
	v_cvt_pk_f16_f32 v19, v2, v3
	v_add_f32_e32 v2, v25, v43
	v_cvt_pk_f16_f32 v4, v4, v5
	v_cvt_pk_f16_f32 v5, v6, v7
	v_cvt_pk_f16_f32 v6, v8, v2
	s_nop 1
	v_permlane32_swap_b32_e32 v4, v6
	v_permlane32_swap_b32_e32 v19, v5
	s_nop 0
	v_add_u32_e32 v130, s4, v54
	v_lshlrev_b64 v[2:3], 5, v[130:131]
	v_lshl_add_u64 v[2:3], v[0:1], 0, v[2:3]
	global_store_dwordx4 v[2:3], v[34:37], off
	s_waitcnt lgkmcnt(1)
	v_mov_b32_e32 v3, v4
	v_mov_b32_e32 v4, v6
	s_waitcnt lgkmcnt(0)
	v_mov_b32_e32 v6, v5
	v_cndmask_b32_e64 v7, v120, v6, s[0:1]
	v_cndmask_b32_e64 v5, v121, v4, s[0:1]
	v_mov_b32_e32 v2, v19
	v_bfi_b32 v5, s2, v4, v5
	v_bfi_b32 v4, s2, v7, v6
	ds_read2st64_b32 v[6:7], v18 offset0:8 offset1:9
	ds_read2st64_b32 v[8:9], v18 offset0:12 offset1:13
	ds_read2st64_b32 v[10:11], v18 offset0:14 offset1:15
	ds_read2st64_b32 v[14:15], v18 offset0:10 offset1:11
	s_waitcnt lgkmcnt(3)
	v_add_f32_e32 v6, v26, v6
	v_add_f32_e32 v7, v27, v7
	s_waitcnt lgkmcnt(2)
	v_add_f32_e32 v8, v30, v8
	v_add_f32_e32 v9, v31, v9
	s_waitcnt lgkmcnt(1)
	v_add_f32_e32 v10, v32, v10
	s_waitcnt lgkmcnt(0)
	v_add_f32_e32 v12, v28, v14
	v_add_f32_e32 v13, v29, v15
	v_cvt_pk_f16_f32 v14, v6, v7
	v_add_f32_e32 v6, v33, v11
	v_cvt_pk_f16_f32 v12, v12, v13
	v_cvt_pk_f16_f32 v8, v8, v9
	v_cvt_pk_f16_f32 v9, v10, v6
	s_nop 1
	v_permlane32_swap_b32_e32 v12, v9
	v_permlane32_swap_b32_e32 v14, v8
	s_nop 0
	v_add_u32_e32 v130, s5, v55
	v_lshlrev_b64 v[6:7], 5, v[130:131]
	v_lshl_add_u64 v[6:7], v[0:1], 0, v[6:7]
	global_store_dwordx4 v[6:7], v[2:5], off
	s_waitcnt lgkmcnt(0)
	v_mov_b32_e32 v6, v8
	v_cndmask_b32_e64 v7, v120, v6, s[0:1]
	v_mov_b32_e32 v4, v9
	v_cndmask_b32_e64 v5, v121, v4, s[0:1]
	v_add_u32_e32 v130, s6, v54
	v_bfi_b32 v5, s2, v4, v5
	v_bfi_b32 v4, s2, v7, v6
	v_lshlrev_b64 v[6:7], 5, v[130:131]
	v_mov_b32_e32 v3, v12
	v_mov_b32_e32 v2, v14
	v_lshl_add_u64 v[0:1], v[0:1], 0, v[6:7]
	global_store_dwordx4 v[0:1], v[2:5], off
	s_endpgm
